# v69 variant: five-unit workgroups run plain, gelu, gelu-stat, sigmoid, sigmoid; converting workgroups rope, rope, sigmoid, sigmoid
# speedup vs baseline: 1.0049x; 1.0049x over previous
;     __device__ bool next(int i, Unit& u) const { if (!base.next(i >> 1, u)) return false; if (i & 1) { u.pm += MTOK / BM; u.pn += DM / BM; } return true; }
;   __device__ __forceinline__ bool next(int i,AttnUnit&u)const{ if(i>=2||vcu>=256)return false; const int s=vcu&3; u.bh=vcu>>2; u.qb=(i==0)?7-s:s; return true; }
;     __host__ __device__ bool next(int i, Unit& u) const {
;         const int L = i * G + c; if (L >= nwg) return false;
;         int wgid = L; { const int q = nwg / NXCD, r = nwg % NXCD, xcd = wgid % NXCD, off = wgid / NXCD; wgid = (xcd < r ? xcd * (q + 1) : r * (q + 1) + (xcd - r) * q) + off; }
;         const int nig = WGM * nN, gid = wgid / nig, fm = gid * WGM, gsz = (nM - fm) < WGM ? (nM - fm) : WGM;
;         u.pm = fm + ((wgid % nig) % gsz); u.pn = (wgid % nig) / gsz; u.half = 0; return true;
.LBB0_382:
	s_ashr_i32 s4, s21, 31
	s_lshr_b32 s4, s4, 29
	s_add_i32 s4, s21, s4
	s_ashr_i32 s5, s4, 3
	s_and_b32 s4, s4, -8
	s_sub_i32 s4, s21, s4
	s_cmp_lt_i32 s4, 0
	s_movk_i32 s6, 0x91
	s_cselect_b32 s6, s6, 0x90
	s_mul_i32 s4, s4, s6
	s_add_i32 s4, s4, s5
	s_mul_hi_i32 s5, s4, 0x38e38e39
	s_lshr_b32 s6, s5, 31
	s_ashr_i32 s5, s5, 5
	s_add_i32 s5, s5, s6
	s_lshl_b32 s6, s5, 3
	s_mulk_i32 s5, 0x90
	s_sub_i32 s4, s4, s5
	s_bfe_u32 s5, s4, 0x3001c
	s_add_i32 s5, s4, s5
	s_sext_i32_i16 s7, s5
	s_and_b32 s5, s5, 0xfff8
	s_sub_i32 s4, s4, s5
	s_sext_i32_i16 s4, s4
	s_add_i32 s18, s6, s4
	s_ashr_i32 s70, s7, 3
	s_mul_i32 s4, s70, 5
	s_cmp_lt_u32 s70, 12
	s_cbranch_scc0 .Lpn_hi0
	s_mov_b32 s6, 0x82029128
	s_mov_b32 s7, 0x5a86239
	s_branch .Lpn_go0

;     __device__ bool next(int i, Unit& u) const { if (!base.next(i >> 1, u)) return false; if (i & 1) { u.pm += MTOK / BM; u.pn += DM / BM; } return true; }
;   __device__ __forceinline__ bool next(int i,AttnUnit&u)const{ if(i>=2||vcu>=256)return false; const int s=vcu&3; u.bh=vcu>>2; u.qb=(i==0)?7-s:s; return true; }
;     __host__ __device__ bool next(int i, Unit& u) const {
;         const int L = i * G + c; if (L >= nwg) return false;
;         int wgid = L; { const int q = nwg / NXCD, r = nwg % NXCD, xcd = wgid % NXCD, off = wgid / NXCD; wgid = (xcd < r ? xcd * (q + 1) : r * (q + 1) + (xcd - r) * q) + off; }
;         const int nig = WGM * nN, gid = wgid / nig, fm = gid * WGM, gsz = (nM - fm) < WGM ? (nM - fm) : WGM;
;         u.pm = fm + ((wgid % nig) % gsz); u.pn = (wgid % nig) / gsz; u.half = 0; return true;
; template <class Epi, class Sched, bool ALIGN_EPI = false, bool SP2 = false>
; __device__ __forceinline__ void gemm_phase(PG8_LAS unsigned char* lds, const Gemm g, const Sched& S, const Epi& E) {
;     ...
;         const bool has_next = S.next(ui + 1, nxt);
;         const char* nA = has_next ? (const char*)g.A + (size_t)nxt.pm * tstep + (nxt.half == 2 ? hstep : (size_t)0) : cA; const char* nB = has_next ? (const char*)g.Bt + (size_t)nxt.pn * tstep : cB;
.LBB0_392:
	s_add_i32 s72, s72, 1
	s_mul_i32 s10, s72, s33
	s_add_i32 s10, s10, s21
	s_cmpk_lt_i32 s10, 0x480
	s_cselect_b64 s[64:65], -1, 0
	s_cmpk_gt_i32 s10, 0x47f
	s_cbranch_scc1 .LBB0_394
	s_ashr_i32 s11, s10, 31
	s_lshr_b32 s11, s11, 29
	s_add_i32 s11, s10, s11
	s_ashr_i32 s12, s11, 3
	s_and_b32 s11, s11, -8
	s_sub_i32 s10, s10, s11
	s_cmp_lt_i32 s10, 0
	s_movk_i32 s11, 0x91
	s_cselect_b32 s11, s11, 0x90
	s_mul_i32 s10, s10, s11
	s_add_i32 s10, s10, s12
	s_mul_hi_i32 s11, s10, 0x38e38e39
	s_lshr_b32 s12, s11, 31
	s_ashr_i32 s11, s11, 5
	s_add_i32 s11, s11, s12
	s_lshl_b32 s12, s11, 3
	s_mulk_i32 s11, 0x90
	s_sub_i32 s10, s10, s11
	s_bfe_u32 s11, s10, 0x3001c
	s_add_i32 s11, s10, s11
	s_sext_i32_i16 s13, s11
	s_and_b32 s11, s11, 0xfff8
	s_sub_i32 s10, s10, s11
	s_sext_i32_i16 s10, s10
	s_add_i32 s60, s12, s10
	s_ashr_i32 s62, s13, 3
	s_mul_i32 s10, s62, 5
	s_cmp_lt_u32 s62, 12
	s_cbranch_scc0 .Lpn_hi1
	s_mov_b32 s12, 0x82029128
	s_mov_b32 s13, 0x5a86239
	s_branch .Lpn_go1
